# attention: dead zero fills before the fp8 packing of P removed, row-sum update by one fma
# baseline (speedup 1.0000x reference)
.LBB0_709:
	v_cvt_pk_fp8_f32 v141, v2, v25
	v_cvt_pk_fp8_f32 v2, v3, v5
	v_cvt_pk_fp8_f32 v3, v0, v4
	v_cvt_pk_fp8_f32 v2, v6, v8 op_sel:[0,0,1]
	v_cvt_pk_fp8_f32 v3, v7, v9 op_sel:[0,0,1]
	v_cvt_pk_fp8_f32 v4, v21, v24
	v_cvt_pk_fp8_f32 v5, v20, v23
	v_cvt_pk_fp8_f32 v6, v100, v104
	v_cvt_pk_fp8_f32 v7, v99, v101
	v_cvt_pk_fp8_f32 v8, v108, v121
	v_cvt_pk_fp8_f32 v9, v107, v109
	v_cvt_pk_fp8_f32 v140, v22, v28
	v_cvt_pk_fp8_f32 v142, v113, v115
	v_cvt_pk_fp8_f32 v143, v112, v114
	v_cvt_pk_fp8_f32 v144, v128, v131
	v_cvt_pk_fp8_f32 v145, v120, v129
	v_cvt_pk_fp8_f32 v146, v135, v136
	v_cvt_pk_fp8_f32 v147, v134, v125
	v_cvt_pk_fp8_f32 v4, v29, v97 op_sel:[0,0,1]
	v_cvt_pk_fp8_f32 v5, v30, v98 op_sel:[0,0,1]
	v_cvt_pk_fp8_f32 v6, v102, v105 op_sel:[0,0,1]
	v_cvt_pk_fp8_f32 v7, v103, v106 op_sel:[0,0,1]
	v_cvt_pk_fp8_f32 v8, v110, v111 op_sel:[0,0,1]
	v_cvt_pk_fp8_f32 v9, v123, v124 op_sel:[0,0,1]
	v_cvt_pk_fp8_f32 v140, v26, v31 op_sel:[0,0,1]
	v_cvt_pk_fp8_f32 v141, v27, v96 op_sel:[0,0,1]
	v_cvt_pk_fp8_f32 v142, v116, v118 op_sel:[0,0,1]
	v_cvt_pk_fp8_f32 v143, v117, v119 op_sel:[0,0,1]
	v_cvt_pk_fp8_f32 v144, v122, v132 op_sel:[0,0,1]
	v_cvt_pk_fp8_f32 v145, v130, v133 op_sel:[0,0,1]
	v_cvt_pk_fp8_f32 v146, v126, v127 op_sel:[0,0,1]
	v_cvt_pk_fp8_f32 v147, v137, v138 op_sel:[0,0,1]
	s_mul_i32 s5, s72, 0x4800
	v_permlane32_swap_b32_e32 v2, v3
	v_permlane32_swap_b32_e32 v4, v5
	v_permlane32_swap_b32_e32 v6, v7
	v_permlane32_swap_b32_e32 v8, v9
	v_add_u32_e32 v0, s5, v214
	v_permlane32_swap_b32_e32 v140, v141
	v_permlane32_swap_b32_e32 v142, v143
	v_permlane32_swap_b32_e32 v144, v145
	v_permlane32_swap_b32_e32 v146, v147
	s_setprio 1
	ds_read_b128 v[20:23], v0
	ds_read_b128 v[24:27], v0 offset:16
	s_andn2_b64 vcc, exec, s[42:43]
	s_waitcnt lgkmcnt(0)
	v_mfma_f32_32x32x64_f8f6f4 v[80:95], v[140:147], v[20:27], v[80:95]
	ds_read_b128 v[20:23], v0 offset:4608
	ds_read_b128 v[24:27], v0 offset:4624
	s_waitcnt lgkmcnt(0)
	v_mfma_f32_32x32x64_f8f6f4 v[64:79], v[140:147], v[20:27], v[64:79]
	ds_read_b128 v[20:23], v0 offset:9216
	ds_read_b128 v[24:27], v0 offset:9232
	s_waitcnt lgkmcnt(0)
	v_mfma_f32_32x32x64_f8f6f4 v[32:47], v[140:147], v[20:27], v[32:47]
	ds_read_b128 v[20:23], v0 offset:13824
	ds_read_b128 v[24:27], v0 offset:13840
	s_waitcnt lgkmcnt(0)
	v_mfma_f32_32x32x64_f8f6f4 v[48:63], v[140:147], v[20:27], v[48:63]
	s_cbranch_vccnz .LBB0_711
	ds_read_b128 v[20:23], v0 offset:64
	ds_read_b128 v[24:27], v0 offset:80
	s_waitcnt lgkmcnt(0)
	v_mfma_f32_32x32x64_f8f6f4 v[80:95], v[2:9], v[20:27], v[80:95]
	ds_read_b128 v[20:23], v0 offset:4672
	ds_read_b128 v[24:27], v0 offset:4688
	s_waitcnt lgkmcnt(0)
	v_mfma_f32_32x32x64_f8f6f4 v[64:79], v[2:9], v[20:27], v[64:79]
	ds_read_b128 v[20:23], v0 offset:9280
	ds_read_b128 v[24:27], v0 offset:9296
	s_waitcnt lgkmcnt(0)
	v_mfma_f32_32x32x64_f8f6f4 v[32:47], v[2:9], v[20:27], v[32:47]
	ds_read_b128 v[20:23], v0 offset:13888
	ds_read_b128 v[24:27], v0 offset:13904
	s_waitcnt lgkmcnt(0)
	v_mfma_f32_32x32x64_f8f6f4 v[48:63], v[2:9], v[20:27], v[48:63]
.LBB0_711:
	v_add_f32_e32 v0, v18, v19
	v_fma_f32 v212, v212, v17, v0
	s_setprio 0
